# prologue RMSNorm loop: gain loads hoisted out of the row loop
# baseline (speedup 1.0000x reference)
; __device__ __forceinline__ unsigned pk2(float lo, float hi) { return f2bf(lo) | (f2bf(hi) << 16); }
; __device__ __forceinline__ float rms_row_load(const float* xrow, int lane, f32x4 (&v)[8]) {
;     const f32x4* xr = (const f32x4*)xrow + lane; float s = 0.f;
; #pragma unroll
;     for (int j = 0; j < 8; ++j) { v[j] = xr[64 * j]; s += (v[j].x * v[j].x + v[j].y * v[j].y) + (v[j].z * v[j].z + v[j].w * v[j].w); }
;     return 1.0f / sqrtf(wave_sum(s) * (1.0f / D) + EPS);
; }
; __device__ __forceinline__ void rms_row_to_bf16(const float* xrow, const float* gain, bf16* orow, int lane) {
;     f32x4 v[8]; const float rstd = rms_row_load(xrow, lane, v);
;     const f32x4* gr = (const f32x4*)gain + lane; unsigned long long* o8 = (unsigned long long*)orow + lane;
; #pragma unroll
;     for (int j = 0; j < 8; ++j) { const f32x4 g = gr[64 * j]; o8[64 * j] = (unsigned long long)pk2(v[j].x * rstd * g.x, v[j].y * rstd * g.y) | ((unsigned long long)pk2(v[j].z * rstd * g.z, v[j].w * rstd * g.w) << 32); }
; __global__ void __launch_bounds__(NWAVES * 64, 2) trunk_fwd(Args args) {
;     ...
;         for (int m = gw; m < M; m += ngw) rms_row_to_bf16(args.in[I_X] + (size_t)m * D, args.in[I_NMIX], Hb + (size_t)m * D, lane);
.LBB0_65:
	s_or_b64 exec, exec, s[4:5]
	v_readlane_b32 s2, v250, 5
	s_add_i32 s12, s3, s2
	s_cmpk_gt_i32 s12, 0x1fff
	s_cbranch_scc1 .LBB0_68
	v_mbcnt_lo_u32_b32 v2, -1, 0
	v_mbcnt_hi_u32_b32 v2, -1, v2
	v_and_b32_e32 v3, 64, v2
	v_add_u32_e32 v3, 64, v3
	v_xor_b32_e32 v4, 1, v2
	v_cmp_lt_i32_e32 vcc, v4, v3
	s_load_dwordx4 s[4:7], s[0:1], 0x0
	s_ashr_i32 s13, s12, 31
	v_cndmask_b32_e32 v4, v2, v4, vcc
	v_lshlrev_b32_e32 v32, 2, v4
	v_xor_b32_e32 v4, 2, v2
	v_cmp_lt_i32_e32 vcc, v4, v3
	s_mov_b64 s[14:15], 0x1c00
	s_mov_b32 s3, 0xf800000
	v_cndmask_b32_e32 v4, v2, v4, vcc
	v_lshlrev_b32_e32 v33, 2, v4
	v_xor_b32_e32 v4, 4, v2
	v_cmp_lt_i32_e32 vcc, v4, v3
	v_mov_b32_e32 v38, 0x260
	s_nop 0
	v_cndmask_b32_e32 v4, v2, v4, vcc
	v_lshlrev_b32_e32 v34, 2, v4
	v_xor_b32_e32 v4, 8, v2
	v_cmp_lt_i32_e32 vcc, v4, v3
	s_nop 1
	v_cndmask_b32_e32 v4, v2, v4, vcc
	v_lshlrev_b32_e32 v35, 2, v4
	v_xor_b32_e32 v4, 16, v2
	v_cmp_lt_i32_e32 vcc, v4, v3
	s_nop 1
	v_cndmask_b32_e32 v4, v2, v4, vcc
	v_lshlrev_b32_e32 v36, 2, v4
	v_xor_b32_e32 v4, 32, v2
	v_cmp_lt_i32_e32 vcc, v4, v3
	v_mov_b32_e32 v3, 0
	v_mov_b32_e32 v5, v3
	v_cndmask_b32_e32 v2, v2, v4, vcc
	v_lshlrev_b32_e32 v37, 2, v2
	v_lshlrev_b32_e32 v2, 4, v1
	s_waitcnt lgkmcnt(0)
	v_lshl_add_u64 v[18:19], s[6:7], 0, v[2:3]
	s_mov_b64 s[6:7], 0x1000
	v_lshl_add_u64 v[20:21], v[18:19], 0, s[6:7]
	s_mov_b64 s[6:7], 0x1400
	v_lshl_add_u64 v[22:23], v[18:19], 0, s[6:7]
	s_mov_b64 s[6:7], 0x1800
	v_lshl_add_u64 v[24:25], v[18:19], 0, s[6:7]
	s_lshl_b64 s[6:7], s[12:13], 12
	s_add_u32 s6, s30, s6
	v_lshlrev_b32_e32 v4, 3, v1
	s_addc_u32 s7, s31, s7
	v_lshl_add_u64 v[4:5], s[6:7], 0, v[4:5]
	s_mov_b64 s[6:7], 0x34da1e00
	s_ashr_i32 s77, s76, 31
	v_lshl_add_u64 v[28:29], v[4:5], 0, s[6:7]
	s_lshl_b64 s[6:7], s[76:77], 12
	s_lshl_b64 s[16:17], s[12:13], 13
	s_add_u32 s4, s4, s16
	s_addc_u32 s5, s5, s17
	v_lshl_add_u64 v[2:3], s[4:5], 0, v[2:3]
	v_lshl_add_u64 v[26:27], v[18:19], 0, s[14:15]
	v_lshl_add_u64 v[30:31], v[2:3], 0, s[14:15]
	s_lshl_b64 s[14:15], s[76:77], 13
	v_mov_b32_e32 v1, 0x3727c5ac
	s_movk_i32 s13, 0x7fff
	s_mov_b32 s16, 0xffff0000
	global_load_dwordx4 v[100:103], v[18:19], off offset:1024
	global_load_dwordx4 v[104:107], v[18:19], off offset:2048
	global_load_dwordx4 v[108:111], v[18:19], off offset:3072
	global_load_dwordx4 v[112:115], v[20:21], off
	global_load_dwordx4 v[116:119], v[22:23], off
	global_load_dwordx4 v[120:123], v[24:25], off
	global_load_dwordx4 v[124:127], v[26:27], off
.LBB0_67:
	global_load_dwordx4 v[14:17], v[30:31], off offset:-3072
	global_load_dwordx4 v[10:13], v[30:31], off offset:-2048
	global_load_dwordx4 v[6:9], v[30:31], off offset:-1024
	global_load_dwordx4 v[2:5], v[30:31], off
	v_add_co_u32_e32 v60, vcc, 0xfffff000, v30
	global_load_dwordx4 v[40:43], v[18:19], off
	s_nop 0
	v_addc_co_u32_e32 v61, vcc, -1, v31, vcc
	global_load_dwordx4 v[44:47], v[60:61], off offset:-3072
	global_load_dwordx4 v[48:51], v[60:61], off offset:-2048
	global_load_dwordx4 v[52:55], v[60:61], off offset:-1024
	global_load_dwordx4 v[56:59], v[30:31], off offset:-4096
	s_add_i32 s12, s12, s76
	s_cmpk_lt_i32 s12, 0x2000
	v_lshl_add_u64 v[30:31], v[30:31], 0, s[14:15]
	s_waitcnt vmcnt(8)
	v_mul_f32_e32 v39, v15, v15
	v_mul_f32_e32 v60, v17, v17
	s_waitcnt vmcnt(7)
	v_mul_f32_e32 v61, v11, v11
	v_mul_f32_e32 v62, v13, v13
	s_waitcnt vmcnt(6)
	v_mul_f32_e32 v63, v7, v7
	v_mul_f32_e32 v64, v9, v9
	s_waitcnt vmcnt(5)
	v_mul_f32_e32 v65, v3, v3
	v_mul_f32_e32 v66, v5, v5
	v_fmac_f32_e32 v39, v14, v14
	v_fmac_f32_e32 v60, v16, v16
	v_fmac_f32_e32 v61, v10, v10
	v_fmac_f32_e32 v62, v12, v12
	v_fmac_f32_e32 v63, v6, v6
	v_fmac_f32_e32 v64, v8, v8
	v_fmac_f32_e32 v65, v2, v2
	v_fmac_f32_e32 v66, v4, v4
	s_waitcnt vmcnt(3)
	v_mul_f32_e32 v67, v45, v45
	v_mul_f32_e32 v68, v47, v47
	v_add_f32_e32 v39, v39, v60
	s_waitcnt vmcnt(2)
	v_mul_f32_e32 v60, v49, v49
	v_add_f32_e32 v61, v61, v62
	v_mul_f32_e32 v62, v51, v51
	v_add_f32_e32 v63, v63, v64
	v_add_f32_e32 v64, v65, v66
	s_waitcnt vmcnt(1)
	v_mul_f32_e32 v65, v53, v53
	v_mul_f32_e32 v66, v55, v55
	v_fmac_f32_e32 v67, v44, v44
	v_fmac_f32_e32 v68, v46, v46
	v_fmac_f32_e32 v60, v48, v48
	v_fmac_f32_e32 v62, v50, v50
	s_waitcnt vmcnt(0)
	v_mul_f32_e32 v69, v57, v57
	v_mul_f32_e32 v70, v59, v59
	v_fmac_f32_e32 v65, v52, v52
	v_fmac_f32_e32 v66, v54, v54
	v_add_f32_e32 v67, v67, v68
	v_add_f32_e32 v60, v60, v62
	v_fmac_f32_e32 v69, v56, v56
	v_fmac_f32_e32 v70, v58, v58
	v_add_f32_e32 v62, v65, v66
	v_add_f32_e32 v60, v67, v60
	v_add_f32_e32 v65, v69, v70
	v_add_f32_e32 v60, v60, v62
	v_add_f32_e32 v60, v60, v65
	v_add_f32_e32 v39, v60, v39
	v_add_f32_e32 v39, v39, v61
	v_add_f32_e32 v39, v39, v63
	v_add_f32_e32 v39, v39, v64
	ds_bpermute_b32 v60, v32, v39
	s_waitcnt lgkmcnt(0)
	v_add_f32_e32 v39, v39, v60
	ds_bpermute_b32 v60, v33, v39
	s_waitcnt lgkmcnt(0)
	v_add_f32_e32 v39, v39, v60
	ds_bpermute_b32 v60, v34, v39
	s_waitcnt lgkmcnt(0)
	v_add_f32_e32 v39, v39, v60
	ds_bpermute_b32 v60, v35, v39
	s_waitcnt lgkmcnt(0)
	v_add_f32_e32 v39, v39, v60
	ds_bpermute_b32 v60, v36, v39
	s_waitcnt lgkmcnt(0)
	v_add_f32_e32 v39, v39, v60
	ds_bpermute_b32 v60, v37, v39
	s_waitcnt lgkmcnt(0)
; __device__ __forceinline__ unsigned pk2(float lo, float hi) { return f2bf(lo) | (f2bf(hi) << 16); }
; __device__ __forceinline__ float rms_row_load(const float* xrow, int lane, f32x4 (&v)[8]) {
;     ...
;     return 1.0f / sqrtf(wave_sum(s) * (1.0f / D) + EPS);
; }
; __device__ __forceinline__ void rms_row_to_bf16(const float* xrow, const float* gain, bf16* orow, int lane) {
;     f32x4 v[8]; const float rstd = rms_row_load(xrow, lane, v);
;     const f32x4* gr = (const f32x4*)gain + lane; unsigned long long* o8 = (unsigned long long*)orow + lane;
; #pragma unroll
;     for (int j = 0; j < 8; ++j) { const f32x4 g = gr[64 * j]; o8[64 * j] = (unsigned long long)pk2(v[j].x * rstd * g.x, v[j].y * rstd * g.y) | ((unsigned long long)pk2(v[j].z * rstd * g.z, v[j].w * rstd * g.w) << 32); }
	v_add_f32_e32 v39, v39, v60
	v_fmamk_f32 v39, v39, 0x3a000000, v1
	v_mul_f32_e32 v60, 0x4f800000, v39
	v_cmp_gt_f32_e32 vcc, s3, v39
	s_nop 1
	v_cndmask_b32_e32 v39, v39, v60, vcc
	v_sqrt_f32_e32 v60, v39
	s_nop 0
	v_add_u32_e32 v61, -1, v60
	v_add_u32_e32 v62, 1, v60
	v_fma_f32 v63, -v61, v60, v39
	v_fma_f32 v64, -v62, v60, v39
	v_cmp_ge_f32_e64 s[4:5], 0, v63
	s_nop 1
	v_cndmask_b32_e64 v60, v60, v61, s[4:5]
	v_cmp_lt_f32_e64 s[4:5], 0, v64
	s_nop 1
	v_cndmask_b32_e64 v60, v60, v62, s[4:5]
	v_mul_f32_e32 v61, 0x37800000, v60
	v_cndmask_b32_e32 v60, v60, v61, vcc
	v_cmp_class_f32_e32 vcc, v39, v38
	s_nop 1
	v_cndmask_b32_e32 v39, v60, v39, vcc
	v_div_scale_f32 v60, s[4:5], v39, v39, 1.0
	v_rcp_f32_e32 v62, v60
	v_div_scale_f32 v61, vcc, 1.0, v39, 1.0
	v_fma_f32 v63, -v60, v62, 1.0
	v_fmac_f32_e32 v62, v63, v62
	v_mul_f32_e32 v63, v61, v62
	v_fma_f32 v64, -v60, v63, v61
	v_fmac_f32_e32 v63, v64, v62
	v_fma_f32 v60, -v60, v63, v61
	v_div_fmas_f32 v60, v60, v62, v63
	v_div_fixup_f32 v39, v60, v39, 1.0
	v_mul_f32_e32 v44, v44, v39
	v_mul_f32_e32 v46, v46, v39
	v_mul_f32_e32 v45, v45, v39
	v_mul_f32_e32 v47, v47, v39
	v_mul_f32_e32 v40, v40, v44
	v_mul_f32_e32 v42, v42, v46
	v_mul_f32_e32 v41, v41, v45
	v_mul_f32_e32 v43, v43, v47
	v_bfe_u32 v44, v40, 16, 1
	v_bfe_u32 v46, v42, 16, 1
	v_bfe_u32 v45, v41, 16, 1
	v_bfe_u32 v47, v43, 16, 1
	v_add3_u32 v40, v40, v44, s13
	v_add3_u32 v42, v42, v46, s13
	v_add3_u32 v41, v41, v45, s13
	v_add3_u32 v43, v43, v47, s13
	v_lshrrev_b32_e32 v40, 16, v40
	v_lshrrev_b32_e32 v42, 16, v42
	v_and_or_b32 v40, v41, s16, v40
	v_and_or_b32 v41, v43, s16, v42
	global_store_dwordx2 v[28:29], v[40:41], off offset:-3584
	v_mul_f32_e32 v48, v48, v39
	v_mul_f32_e32 v50, v50, v39
	v_mul_f32_e32 v49, v49, v39
	v_mul_f32_e32 v44, v51, v39
	v_mul_f32_e32 v14, v14, v39
	v_mul_f32_e32 v16, v16, v39
	v_mul_f32_e32 v15, v15, v39
	v_mul_f32_e32 v17, v17, v39
	v_mul_f32_e32 v10, v10, v39
	v_mul_f32_e32 v12, v12, v39
	v_mul_f32_e32 v11, v11, v39
	v_mul_f32_e32 v13, v13, v39
	v_mul_f32_e32 v6, v6, v39
	v_mul_f32_e32 v8, v8, v39
	v_mul_f32_e32 v7, v7, v39
	v_mul_f32_e32 v9, v9, v39
	v_mul_f32_e32 v2, v2, v39
	v_mul_f32_e32 v4, v4, v39
	v_mul_f32_e32 v3, v3, v39
	v_mul_f32_e32 v5, v5, v39
	v_mul_f32_e32 v40, v100, v48
	v_mul_f32_e32 v42, v102, v50
	v_mul_f32_e32 v41, v101, v49
	v_mul_f32_e32 v43, v103, v44
	v_bfe_u32 v44, v40, 16, 1
	v_bfe_u32 v46, v42, 16, 1
	v_bfe_u32 v45, v41, 16, 1
	v_bfe_u32 v47, v43, 16, 1
	v_add3_u32 v40, v40, v44, s13
	v_add3_u32 v42, v42, v46, s13
	v_add3_u32 v41, v41, v45, s13
	v_add3_u32 v43, v43, v47, s13
	v_lshrrev_b32_e32 v40, 16, v40
	v_lshrrev_b32_e32 v42, 16, v42
	v_and_or_b32 v40, v41, s16, v40
	v_and_or_b32 v41, v43, s16, v42
	global_store_dwordx2 v[28:29], v[40:41], off offset:-3072
	v_mul_f32_e32 v44, v52, v39
	v_mul_f32_e32 v46, v54, v39
	v_mul_f32_e32 v45, v53, v39
	v_mul_f32_e32 v47, v55, v39
	v_mul_f32_e32 v40, v104, v44
	v_mul_f32_e32 v42, v106, v46
	v_mul_f32_e32 v41, v105, v45
	v_mul_f32_e32 v43, v107, v47
	v_bfe_u32 v44, v40, 16, 1
	v_bfe_u32 v46, v42, 16, 1
	v_bfe_u32 v45, v41, 16, 1
	v_bfe_u32 v47, v43, 16, 1
	v_add3_u32 v40, v40, v44, s13
	v_add3_u32 v42, v42, v46, s13
	v_add3_u32 v41, v41, v45, s13
	v_add3_u32 v43, v43, v47, s13
	v_lshrrev_b32_e32 v40, 16, v40
	v_lshrrev_b32_e32 v42, 16, v42
	v_and_or_b32 v40, v41, s16, v40
	v_and_or_b32 v41, v43, s16, v42
	global_store_dwordx2 v[28:29], v[40:41], off offset:-2560
	v_mul_f32_e32 v44, v56, v39
	v_mul_f32_e32 v46, v58, v39
	v_mul_f32_e32 v45, v57, v39
	v_mul_f32_e32 v47, v59, v39
	v_mul_f32_e32 v40, v44, v108
	v_mul_f32_e32 v42, v46, v110
	v_mul_f32_e32 v41, v45, v109
	v_mul_f32_e32 v43, v47, v111
	v_bfe_u32 v44, v40, 16, 1
	v_bfe_u32 v46, v42, 16, 1
	v_bfe_u32 v45, v41, 16, 1
	v_bfe_u32 v47, v43, 16, 1
	v_add3_u32 v40, v40, v44, s13
	v_add3_u32 v42, v42, v46, s13
	v_add3_u32 v41, v41, v45, s13
	v_add3_u32 v43, v43, v47, s13
	v_lshrrev_b32_e32 v40, 16, v40
	v_lshrrev_b32_e32 v42, 16, v42
	v_and_or_b32 v40, v41, s16, v40
	v_and_or_b32 v41, v43, s16, v42
	global_store_dwordx2 v[28:29], v[40:41], off offset:-2048
	v_mul_f32_e32 v14, v14, v112
	v_mul_f32_e32 v16, v16, v114
	v_mul_f32_e32 v15, v15, v113
	v_mul_f32_e32 v17, v17, v115
	v_bfe_u32 v40, v14, 16, 1
	v_bfe_u32 v42, v16, 16, 1
	v_bfe_u32 v41, v15, 16, 1
	v_bfe_u32 v43, v17, 16, 1
	v_add3_u32 v14, v14, v40, s13
	v_add3_u32 v16, v16, v42, s13
	v_add3_u32 v15, v15, v41, s13
	v_add3_u32 v17, v17, v43, s13
	v_lshrrev_b32_e32 v14, 16, v14
	v_lshrrev_b32_e32 v16, 16, v16
	v_and_or_b32 v14, v15, s16, v14
	v_and_or_b32 v15, v17, s16, v16
	global_store_dwordx2 v[28:29], v[14:15], off offset:-1536
	v_mul_f32_e32 v10, v10, v116
	v_mul_f32_e32 v12, v12, v118
	v_mul_f32_e32 v11, v11, v117
	v_mul_f32_e32 v13, v13, v119
	v_bfe_u32 v14, v10, 16, 1
	v_bfe_u32 v16, v12, 16, 1
	v_bfe_u32 v15, v11, 16, 1
	v_bfe_u32 v17, v13, 16, 1
	v_add3_u32 v10, v10, v14, s13
	v_add3_u32 v12, v12, v16, s13
	v_add3_u32 v11, v11, v15, s13
	v_add3_u32 v13, v13, v17, s13
	v_lshrrev_b32_e32 v10, 16, v10
	v_lshrrev_b32_e32 v12, 16, v12
	v_and_or_b32 v10, v11, s16, v10
	v_and_or_b32 v11, v13, s16, v12
	global_store_dwordx2 v[28:29], v[10:11], off offset:-1024
	v_mul_f32_e32 v6, v6, v120
	v_mul_f32_e32 v8, v8, v122
	v_mul_f32_e32 v7, v7, v121
	v_mul_f32_e32 v9, v9, v123
	v_bfe_u32 v10, v6, 16, 1
	v_bfe_u32 v12, v8, 16, 1
	v_bfe_u32 v11, v7, 16, 1
	v_bfe_u32 v13, v9, 16, 1
	v_add3_u32 v6, v6, v10, s13
	v_add3_u32 v8, v8, v12, s13
	v_add3_u32 v7, v7, v11, s13
	v_add3_u32 v9, v9, v13, s13
	v_lshrrev_b32_e32 v6, 16, v6
	v_lshrrev_b32_e32 v8, 16, v8
	v_and_or_b32 v6, v7, s16, v6
	v_and_or_b32 v7, v9, s16, v8
	global_store_dwordx2 v[28:29], v[6:7], off offset:-512
	v_mul_f32_e32 v2, v2, v124
	v_mul_f32_e32 v4, v4, v126
	v_mul_f32_e32 v3, v3, v125
	v_mul_f32_e32 v5, v5, v127
	v_bfe_u32 v6, v2, 16, 1
	v_bfe_u32 v8, v4, 16, 1
	v_bfe_u32 v7, v3, 16, 1
	v_bfe_u32 v9, v5, 16, 1
	v_add3_u32 v2, v2, v6, s13
	v_add3_u32 v4, v4, v8, s13
	v_add3_u32 v3, v3, v7, s13
	v_add3_u32 v5, v5, v9, s13
	v_lshrrev_b32_e32 v2, 16, v2
	v_lshrrev_b32_e32 v4, 16, v4
	v_and_or_b32 v2, v3, s16, v2
	v_and_or_b32 v3, v5, s16, v4
	global_store_dwordx2 v[28:29], v[2:3], off
	v_lshl_add_u64 v[28:29], v[28:29], 0, s[6:7]
	s_cbranch_scc1 .LBB0_67
